# v9: v8 + static s_setprio 1 for the scan helper waves (younger half)
# baseline (speedup 1.0000x reference)
.LBB0_1719:
	s_setprio 0
	v_readlane_b32 s82, v255, 5
	s_barrier

.LBB0_1737:
	s_and_b64 vcc, exec, s[68:69]
	s_cbranch_vccz .LBB0_1720
	s_setprio 1
	v_or_b32_e32 v2, s72, v1
	v_lshlrev_b32_e32 v2, 2, v2
	s_waitcnt lgkmcnt(0)
	global_load_dword v43, v2, s[38:39]
	global_load_dword v42, v2, s[36:37]
	s_and_saveexec_b64 s[68:69], s[10:11]
	s_xor_b64 s[68:69], exec, s[68:69]
	v_add_u32_e32 v2, 0xffffff00, v194
	v_sub_u32_e32 v3, 0x40ff, v194
	v_cndmask_b32_e64 v2, v3, v2, s[28:29]
	v_lshl_add_u32 v2, s73, 14, v2
	s_andn2_saveexec_b64 s[68:69], s[68:69]
	v_sub_u32_e32 v2, 0xff, v194
	v_cndmask_b32_e64 v2, v2, v194, s[28:29]
	v_lshl_add_u32 v2, s73, 8, v2
	v_add_u32_e32 v2, 0x8000, v2
	s_or_b64 exec, exec, s[68:69]
	v_ashrrev_i32_e32 v3, 31, v2
	v_lshlrev_b64 v[2:3], 11, v[2:3]
	v_or_b32_e32 v2, v2, v162
	s_and_b64 s[68:69], s[28:29], exec
	v_or_b32_e32 v2, s72, v2
	s_cselect_b32 s69, s41, s43
	s_cselect_b32 s68, s40, s42
	v_lshlrev_b64 v[18:19], 1, v[2:3]
	v_lshl_add_u64 v[2:3], s[66:67], 0, v[18:19]
	v_lshl_add_u64 v[6:7], s[68:69], 0, v[18:19]
	v_lshl_add_u64 v[10:11], s[44:45], 0, v[18:19]
	v_lshl_add_u64 v[14:15], s[34:35], 0, v[18:19]
	v_lshl_add_u64 v[18:19], s[46:47], 0, v[18:19]
	global_load_dwordx4 v[2:5], v[2:3], off
	s_nop 0
	global_load_dwordx4 v[6:9], v[6:7], off
	s_nop 0
	global_load_dwordx4 v[10:13], v[10:11], off
	s_nop 0
	global_load_dwordx4 v[14:17], v[14:15], off
	s_nop 0
	global_load_dwordx4 v[18:21], v[18:19], off
	s_and_saveexec_b64 s[70:71], s[12:13]
	s_xor_b64 s[70:71], exec, s[70:71]
	v_add_u32_e32 v22, 0xffffff00, v199
	v_sub_u32_e32 v23, 0x40ff, v199
	v_cndmask_b32_e64 v22, v23, v22, s[28:29]
	v_lshl_add_u32 v22, s73, 14, v22
	s_andn2_saveexec_b64 s[70:71], s[70:71]
	v_sub_u32_e32 v22, 0xff, v199
	v_cndmask_b32_e64 v22, v22, v199, s[28:29]
	v_lshl_add_u32 v22, s73, 8, v22
	v_add_u32_e32 v22, 0x8000, v22
	s_or_b64 exec, exec, s[70:71]
	v_ashrrev_i32_e32 v23, 31, v22
	v_lshlrev_b64 v[22:23], 11, v[22:23]
	v_or3_b32 v23, v23, 0, 0
	v_or3_b32 v22, v22, v162, s72
	v_lshlrev_b64 v[38:39], 1, v[22:23]
	v_lshl_add_u64 v[22:23], s[66:67], 0, v[38:39]
	v_lshl_add_u64 v[26:27], s[68:69], 0, v[38:39]
	v_lshl_add_u64 v[30:31], s[44:45], 0, v[38:39]
	v_lshl_add_u64 v[34:35], s[34:35], 0, v[38:39]
	v_lshl_add_u64 v[38:39], s[46:47], 0, v[38:39]
	global_load_dwordx4 v[22:25], v[22:23], off
	s_mov_b64 s[70:71], -1
	global_load_dwordx4 v[26:29], v[26:27], off
	s_nop 0
	global_load_dwordx4 v[30:33], v[30:31], off
	s_nop 0
	global_load_dwordx4 v[34:37], v[34:35], off
	s_and_b64 vcc, exec, s[58:59]
	global_load_dwordx4 v[38:41], v[38:39], off
	s_cbranch_vccz .LBB0_1748
	v_add_u32_e32 v44, 0xffffff00, v203
	v_sub_u32_e32 v45, 0x40ff, v203
	v_cndmask_b32_e64 v44, v45, v44, s[28:29]
	v_lshl_add_u32 v44, s73, 14, v44
	s_mov_b64 s[70:71], 0
